# accumulator clearing MFMAs moved to the top of the unit-loop header (overlap with scalar tile-map code)
# baseline (speedup 1.0000x reference)
;     DI bool next(int i, Unit& u) const { u.aux = 0; return tile_map(i, nM, nN, G, c, u.pm, u.pn); }
;     DI size_t a_off(const Unit& u) const { return (size_t)u.pm * astep; }
;     DI size_t b_off(const Unit& u) const { return (size_t)u.pn * bstep; }
;     DI bool next(int i, Unit& u) const { int pn; u.aux = 0; if (!tile_map(i, NTOK / 256, 16, G, c, u.pm, pn)) return false; u.pn = pn < 8 ? pn : pn + 8; return true; }
;     DI size_t a_off(const Unit& u) const { return (size_t)u.pm * (256 * D_ * 2); }
;     DI size_t b_off(const Unit& u) const { return (size_t)u.pn * (256 * D_ * 2); }
;     DI bool next(int i, Unit& u) const { int pn2; if (!tile_map(i, NTOK / 256, 8, G, c, u.pm, pn2)) return false; u.pn = pn2 >> 1; u.aux = pn2 & 1; return true; }
;     DI size_t a_off(const Unit& u) const { return (size_t)u.pm * (256 * D_ * 2) + (size_t)u.aux * (D_ / 2 * 2); }
;     DI size_t b_off(const Unit& u) const { return (size_t)(12 + u.pn) * (256 * D_ * 2) + (size_t)u.aux * (D_ / 2 * 2); }
;     DI bool next(int i, Unit& u) const { u.aux = 0; return tile_map(i, 8, NTOK / 256, G, c, u.pm, u.pn); }
;     DI size_t b_off(const Unit& u) const { return (size_t)u.pn * (256 * D_ * 2); }
; DI bool tile_map(int i, int nM, int nN, int G, int c, int& pm, int& pn) {
;     const int nwg = nM * nN; const long L = (long)i * G + c; if (L >= nwg) return false;
;     int wgid = (int)L; { const int q = nwg / NXCD, r = nwg % NXCD, xcd = wgid % NXCD, off = wgid / NXCD; wgid = (xcd < r ? xcd * (q + 1) : r * (q + 1) + (xcd - r) * q) + off; }
;     const int nig = WGM * nN, gid = wgid / nig, fm = gid * WGM, gsz = (nM - fm) < WGM ? (nM - fm) : WGM;
;     pm = fm + ((wgid % nig) % gsz); pn = (wgid % nig) / gsz; return true;
; template <class Epi, class Sched, bool ALIGN_EPI, bool FP8 = false>
; DI void gemm_phase(LAS unsigned char* lds, const Gemm g, const Sched& S, const Epi& E) {
;     ...
;     for (;;) {
;         const bool has_next = S.next(ui + 1, nxt);
;         const char* nA = has_next ? (const char*)g.A + S.a_off(nxt) : cA; const char* nB = has_next ? (const char*)g.Bt + S.b_off(nxt) : cB;
;     ...
; #pragma unroll
;         for (int a = 0; a < 2; ++a)
; #pragma unroll
;             for (int b = 0; b < 2; ++b)
; #pragma unroll
;                 for (int m = 0; m < 4; ++m)
; #pragma unroll
;                     for (int n = 0; n < 2; ++n) acc[a][b][m][n] = (f32x4){0.f, 0.f, 0.f, 0.f};
.LBB0_562:
	v_mov_b32_e32 v124, 0
	v_mov_b32_e32 v125, 0
	v_mov_b32_e32 v126, 0
	v_mov_b32_e32 v127, 0
	s_nop 1
	v_mfma_f32_32x32x16_bf16 v[0:15], v[124:127], v[124:127], 0
	v_mfma_f32_32x32x16_bf16 v[16:31], v[124:127], v[124:127], 0
	v_mfma_f32_32x32x16_bf16 v[32:47], v[124:127], v[124:127], 0
	v_mfma_f32_32x32x16_bf16 v[48:63], v[124:127], v[124:127], 0
	v_mfma_f32_32x32x16_bf16 v[64:79], v[124:127], v[124:127], 0
	v_mfma_f32_32x32x16_bf16 v[80:95], v[124:127], v[124:127], 0
	v_mfma_f32_32x32x16_bf16 v[96:111], v[124:127], v[124:127], 0
	v_mfma_f32_16x16x32_bf16 v[112:115], v[124:127], v[124:127], 0
	v_mfma_f32_16x16x32_bf16 v[116:119], v[124:127], v[124:127], 0
	v_mfma_f32_16x16x32_bf16 v[120:123], v[124:127], v[124:127], 0
	s_add_i32 s39, s39, 1
	s_mul_i32 s4, s39, s91
	s_mul_hi_u32 s5, s39, s34
	s_add_i32 s5, s5, s4
	s_mul_i32 s4, s39, s34
	s_add_u32 s58, s4, s2
	s_addc_u32 s59, s5, s3
	v_cmp_gt_i64_e32 vcc, s[58:59], v[130:131]
	v_cmp_lt_i64_e64 s[4:5], s[58:59], v[128:129]
	s_cbranch_vccnz .LBB0_568
	s_ashr_i32 s54, s58, 31
	s_lshr_b32 s54, s54, 29
	s_add_i32 s56, s58, s54
	s_and_b32 s54, s56, -8
	s_sub_i32 s57, s58, s54
	s_cmp_gt_i32 s57, -1
	s_mov_b64 s[54:55], -1
	s_cbranch_scc0 .LBB0_565
	s_lshl_b32 s58, s57, 5
	s_mov_b64 s[54:55], 0

; #define PG8_BAR __builtin_amdgcn_s_barrier()
;     DI int nt(const Unit& u) const { return (u.aux & 8) ? PLED / 64 : ((u.aux & 4) ? (D_ / 2) / 64 : D_ / 64); }
; DI bool tile_map(int i, int nM, int nN, int G, int c, int& pm, int& pn) {
;     const int nwg = nM * nN; const long L = (long)i * G + c; if (L >= nwg) return false;
;     int wgid = (int)L; { const int q = nwg / NXCD, r = nwg % NXCD, xcd = wgid % NXCD, off = wgid / NXCD; wgid = (xcd < r ? xcd * (q + 1) : r * (q + 1) + (xcd - r) * q) + off; }
;     const int nig = WGM * nN, gid = wgid / nig, fm = gid * WGM, gsz = (nM - fm) < WGM ? (nM - fm) : WGM;
;     pm = fm + ((wgid % nig) % gsz); pn = (wgid % nig) / gsz; return true;
; template <class Epi, class Sched, bool ALIGN_EPI, bool FP8 = false>
; DI void gemm_phase(LAS unsigned char* lds, const Gemm g, const Sched& S, const Epi& E) {
;     ...
; #pragma unroll
;         for (int a = 0; a < 2; ++a)
; #pragma unroll
;             for (int b = 0; b < 2; ++b)
; #pragma unroll
;                 for (int m = 0; m < 4; ++m)
; #pragma unroll
;                     for (int n = 0; n < 2; ++n) acc[a][b][m][n] = (f32x4){0.f, 0.f, 0.f, 0.f};
;         cur = nxt; cA = nA; cB = nB; ++ui;
;         if constexpr (sched_vark<Sched>::value) nt = S.nt(cur);
;         if constexpr (ALIGN_EPI) { if (wr == 1) PG8_BAR; }
.LBB0_567:
	s_ashr_i32 s54, s56, 3
	s_add_i32 s54, s58, s54
	s_ashr_i32 s55, s54, 31
	s_lshr_b32 s55, s55, 26
	s_add_i32 s55, s54, s55
	s_ashr_i32 s56, s55, 6
	s_lshl_b32 s56, s56, 3
	s_sub_i32 s57, 32, s56
	s_min_i32 s57, s57, 8
	s_abs_i32 s58, s57
	v_cvt_f32_u32_e32 v255, s58
	s_sub_i32 s60, 0, s58
	s_andn2_b32 s55, s55, 63
	s_sub_i32 s55, s54, s55
	v_rcp_iflag_f32_e32 v255, v255
	s_abs_i32 s54, s55
	s_xor_b32 s59, s55, s57
	s_ashr_i32 s59, s59, 31
	v_mul_f32_e32 v255, 0x4f7ffffe, v255
	v_cvt_u32_f32_e32 v255, v255
	s_nop 0
	v_readfirstlane_b32 s61, v255
	s_mul_i32 s60, s60, s61
	s_mul_hi_u32 s60, s61, s60
	s_add_i32 s61, s61, s60
	s_mul_hi_u32 s60, s54, s61
	s_mul_i32 s61, s60, s58
	s_sub_i32 s54, s54, s61
	s_add_i32 s68, s60, 1
	s_sub_i32 s61, s54, s58
	s_cmp_ge_u32 s54, s58
	s_cselect_b32 s60, s68, s60
	s_cselect_b32 s54, s61, s54
	s_add_i32 s61, s60, 1
	s_cmp_ge_u32 s54, s58
	s_cselect_b32 s54, s61, s60
	s_xor_b32 s54, s54, s59
	s_sub_i32 s54, s54, s59
	s_mul_i32 s57, s54, s57
	s_sub_i32 s55, s55, s57
	s_add_i32 s56, s56, s55
.LBB0_568:
	s_ashr_i32 s57, s56, 31
	s_lshl_b64 s[58:59], s[56:57], 20
	s_add_u32 s58, s17, s58
	s_addc_u32 s59, s35, s59
	s_and_b64 s[60:61], s[4:5], exec
	s_cselect_b32 s57, s59, s65
	s_cselect_b32 s93, s58, s64
	s_ashr_i32 s55, s54, 31
	s_lshl_b64 s[60:61], s[54:55], 20
	s_add_u32 s60, s36, s60
	s_addc_u32 s61, s37, s61
	s_and_b64 s[68:69], s[4:5], exec
	s_cselect_b32 s55, s61, s67
	s_cselect_b32 s94, s60, s66
	s_add_u32 s95, s66, 0x100
	s_addc_u32 s96, s67, 0
	s_mov_b32 s97, -2
	s_waitcnt vmcnt(15)
	s_waitcnt vmcnt(14)
	s_waitcnt vmcnt(13)
	s_waitcnt vmcnt(12)
	s_waitcnt vmcnt(11)
	s_waitcnt vmcnt(9)
	s_waitcnt vmcnt(8)
	.p2alignl 6, 3212836864

; #define PG8_BAR __builtin_amdgcn_s_barrier()
;     DI bool next(int i, Unit& u) const { u.aux = 0; return tile_map(i, nM, nN, G, c, u.pm, u.pn); }
;     DI size_t a_off(const Unit& u) const { return (size_t)u.pm * astep; }
;     DI size_t b_off(const Unit& u) const { return (size_t)u.pn * bstep; }
;     DI bool next(int i, Unit& u) const { int pn; u.aux = 0; if (!tile_map(i, NTOK / 256, 16, G, c, u.pm, pn)) return false; u.pn = pn < 8 ? pn : pn + 8; return true; }
;     DI size_t a_off(const Unit& u) const { return (size_t)u.pm * (256 * D_ * 2); }
;     DI size_t b_off(const Unit& u) const { return (size_t)u.pn * (256 * D_ * 2); }
;     DI bool next(int i, Unit& u) const { int pn2; if (!tile_map(i, NTOK / 256, 8, G, c, u.pm, pn2)) return false; u.pn = pn2 >> 1; u.aux = pn2 & 1; return true; }
;     DI size_t a_off(const Unit& u) const { return (size_t)u.pm * (256 * D_ * 2) + (size_t)u.aux * (D_ / 2 * 2); }
;     DI bool next(int i, Unit& u) const { u.aux = 0; return tile_map(i, 8, NTOK / 256, G, c, u.pm, u.pn); }
; DI bool tile_map(int i, int nM, int nN, int G, int c, int& pm, int& pn) {
;     const int nwg = nM * nN; const long L = (long)i * G + c; if (L >= nwg) return false;
;     int wgid = (int)L; { const int q = nwg / NXCD, r = nwg % NXCD, xcd = wgid % NXCD, off = wgid / NXCD; wgid = (xcd < r ? xcd * (q + 1) : r * (q + 1) + (xcd - r) * q) + off; }
;     const int nig = WGM * nN, gid = wgid / nig, fm = gid * WGM, gsz = (nM - fm) < WGM ? (nM - fm) : WGM;
;     pm = fm + ((wgid % nig) % gsz); pn = (wgid % nig) / gsz; return true;
; template <class Epi, class Sched, bool ALIGN_EPI, bool FP8 = false>
; DI void gemm_phase(LAS unsigned char* lds, const Gemm g, const Sched& S, const Epi& E) {
;     ...
;     for (;;) {
;         const bool has_next = S.next(ui + 1, nxt);
;         const char* nA = has_next ? (const char*)g.A + S.a_off(nxt) : cA; const char* nB = has_next ? (const char*)g.Bt + S.b_off(nxt) : cB;
;     ...
; #pragma unroll
;         for (int a = 0; a < 2; ++a)
; #pragma unroll
;             for (int b = 0; b < 2; ++b)
; #pragma unroll
;                 for (int m = 0; m < 4; ++m)
; #pragma unroll
;                     for (int n = 0; n < 2; ++n) acc[a][b][m][n] = (f32x4){0.f, 0.f, 0.f, 0.f};
;         cur = nxt; cA = nA; cB = nB; ++ui;
;         if constexpr (sched_vark<Sched>::value) nt = S.nt(cur);
;         if constexpr (ALIGN_EPI) { if (wr == 1) PG8_BAR; }
.LBB0_697:
	v_mov_b32_e32 v124, 0
	v_mov_b32_e32 v125, 0
	v_mov_b32_e32 v126, 0
	v_mov_b32_e32 v127, 0
	s_nop 1
	v_mfma_f32_32x32x16_bf16 v[0:15], v[124:127], v[124:127], 0
	v_mfma_f32_32x32x16_bf16 v[16:31], v[124:127], v[124:127], 0
	v_mfma_f32_32x32x16_bf16 v[32:47], v[124:127], v[124:127], 0
	v_mfma_f32_32x32x16_bf16 v[48:63], v[124:127], v[124:127], 0
	v_mfma_f32_32x32x16_bf16 v[64:79], v[124:127], v[124:127], 0
	v_mfma_f32_32x32x16_bf16 v[80:95], v[124:127], v[124:127], 0
	v_mfma_f32_32x32x16_bf16 v[96:111], v[124:127], v[124:127], 0
	v_mfma_f32_16x16x32_bf16 v[112:115], v[124:127], v[124:127], 0
	v_mfma_f32_16x16x32_bf16 v[116:119], v[124:127], v[124:127], 0
	v_mfma_f32_16x16x32_bf16 v[120:123], v[124:127], v[124:127], 0
	s_add_i32 s39, s39, 1
	s_mul_i32 s4, s39, s63
	s_mul_hi_u32 s5, s39, s34
	s_add_i32 s5, s5, s4
	s_mul_i32 s4, s39, s34
	s_add_u32 s18, s4, s2
	s_addc_u32 s19, s5, s45
	v_cmp_gt_i64_e32 vcc, s[18:19], v[130:131]
	v_cmp_lt_i64_e64 s[4:5], s[18:19], v[128:129]
	s_cbranch_vccnz .LBB0_699
	s_ashr_i32 s12, s18, 31
	s_lshr_b32 s12, s12, 29
	s_add_i32 s12, s18, s12
	s_ashr_i32 s13, s12, 3
	s_and_b32 s12, s12, -8
	s_sub_i32 s12, s18, s12
	s_cmp_lt_i32 s12, 0
	s_cselect_b32 s16, s46, 0xb0
	s_mul_i32 s12, s16, s12
	s_add_i32 s12, s12, s13
	s_mul_hi_i32 s13, s12, 0x2e8ba2e9
	s_lshr_b32 s16, s13, 31
	s_ashr_i32 s13, s13, 6
	s_add_i32 s13, s13, s16
	s_lshl_b32 s16, s13, 3
	s_sub_i32 s17, 32, s16
	s_min_i32 s17, s17, 8
	s_abs_i32 s18, s17
	v_cvt_f32_u32_e32 v255, s18
	s_sub_i32 s20, 0, s18
	s_mulk_i32 s13, 0x160
	s_sub_i32 s13, s12, s13
	v_rcp_iflag_f32_e32 v255, v255
	s_abs_i32 s12, s13
	s_xor_b32 s19, s13, s17
	s_ashr_i32 s19, s19, 31
	v_mul_f32_e32 v255, 0x4f7ffffe, v255
	v_cvt_u32_f32_e32 v255, v255
	s_nop 0
	v_readfirstlane_b32 s21, v255
	s_mul_i32 s20, s20, s21
	s_mul_hi_u32 s20, s21, s20
	s_add_i32 s21, s21, s20
	s_mul_hi_u32 s20, s12, s21
	s_mul_i32 s21, s20, s18
	s_sub_i32 s12, s12, s21
	s_add_i32 s28, s20, 1
	s_sub_i32 s21, s12, s18
	s_cmp_ge_u32 s12, s18
	s_cselect_b32 s20, s28, s20
	s_cselect_b32 s12, s21, s12
	s_add_i32 s21, s20, 1
	s_cmp_ge_u32 s12, s18
	s_cselect_b32 s12, s21, s20
	s_xor_b32 s12, s12, s19
	s_sub_i32 s12, s12, s19
	s_mul_i32 s17, s12, s17
	s_sub_i32 s13, s13, s17
	s_add_i32 s16, s13, s16
.LBB0_699:
	s_ashr_i32 s17, s16, 31
	s_lshl_b64 s[18:19], s[16:17], 20
	s_add_u32 s18, s3, s18
	s_addc_u32 s19, s35, s19
	s_and_b64 s[20:21], s[4:5], exec
	s_cselect_b32 s17, s19, s25
	s_cselect_b32 s67, s18, s24
	s_ashr_i32 s13, s12, 31
	s_lshl_b64 s[20:21], s[12:13], 20
	s_add_u32 s20, s36, s20
	s_addc_u32 s21, s37, s21
	s_and_b64 s[28:29], s[4:5], exec
	s_cselect_b32 s13, s21, s27
	s_cselect_b32 s68, s20, s26
	s_add_u32 s69, s26, 0x100
	s_addc_u32 s70, s27, 0
	s_mov_b32 s71, -2
	.p2alignl 6, 3212836864

;     DI bool next(int i, Unit& u) const { u.aux = 0; return tile_map(i, nM, nN, G, c, u.pm, u.pn); }
;     DI size_t a_off(const Unit& u) const { return (size_t)u.pm * astep; }
;     DI size_t b_off(const Unit& u) const { return (size_t)u.pn * bstep; }
;     DI bool next(int i, Unit& u) const { int pn; u.aux = 0; if (!tile_map(i, NTOK / 256, 16, G, c, u.pm, pn)) return false; u.pn = pn < 8 ? pn : pn + 8; return true; }
;     DI size_t a_off(const Unit& u) const { return (size_t)u.pm * (256 * D_ * 2); }
;     DI size_t b_off(const Unit& u) const { return (size_t)u.pn * (256 * D_ * 2); }
;     DI bool next(int i, Unit& u) const { int pn2; if (!tile_map(i, NTOK / 256, 8, G, c, u.pm, pn2)) return false; u.pn = pn2 >> 1; u.aux = pn2 & 1; return true; }
;     DI size_t a_off(const Unit& u) const { return (size_t)u.pm * (256 * D_ * 2) + (size_t)u.aux * (D_ / 2 * 2); }
;     DI size_t b_off(const Unit& u) const { return (size_t)(12 + u.pn) * (256 * D_ * 2) + (size_t)u.aux * (D_ / 2 * 2); }
;     DI bool next(int i, Unit& u) const { u.aux = 0; return tile_map(i, 8, NTOK / 256, G, c, u.pm, u.pn); }
;     DI size_t b_off(const Unit& u) const { return (size_t)u.pn * (256 * D_ * 2); }
; DI bool tile_map(int i, int nM, int nN, int G, int c, int& pm, int& pn) {
;     const int nwg = nM * nN; const long L = (long)i * G + c; if (L >= nwg) return false;
;     int wgid = (int)L; { const int q = nwg / NXCD, r = nwg % NXCD, xcd = wgid % NXCD, off = wgid / NXCD; wgid = (xcd < r ? xcd * (q + 1) : r * (q + 1) + (xcd - r) * q) + off; }
;     const int nig = WGM * nN, gid = wgid / nig, fm = gid * WGM, gsz = (nM - fm) < WGM ? (nM - fm) : WGM;
;     pm = fm + ((wgid % nig) % gsz); pn = (wgid % nig) / gsz; return true;
; template <class Epi, class Sched, bool ALIGN_EPI, bool FP8 = false>
; DI void gemm_phase(LAS unsigned char* lds, const Gemm g, const Sched& S, const Epi& E) {
;     ...
;     for (;;) {
;         const bool has_next = S.next(ui + 1, nxt);
;         const char* nA = has_next ? (const char*)g.A + S.a_off(nxt) : cA; const char* nB = has_next ? (const char*)g.Bt + S.b_off(nxt) : cB;
;     ...
; #pragma unroll
;         for (int a = 0; a < 2; ++a)
; #pragma unroll
;             for (int b = 0; b < 2; ++b)
; #pragma unroll
;                 for (int m = 0; m < 4; ++m)
; #pragma unroll
;                     for (int n = 0; n < 2; ++n) acc[a][b][m][n] = (f32x4){0.f, 0.f, 0.f, 0.f};
.LBB0_717:
	v_mov_b32_e32 v124, 0
	v_mov_b32_e32 v125, 0
	v_mov_b32_e32 v126, 0
	v_mov_b32_e32 v127, 0
	s_nop 1
	v_mfma_f32_32x32x16_bf16 v[0:15], v[124:127], v[124:127], 0
	v_mfma_f32_32x32x16_bf16 v[16:31], v[124:127], v[124:127], 0
	v_mfma_f32_32x32x16_bf16 v[32:47], v[124:127], v[124:127], 0
	v_mfma_f32_32x32x16_bf16 v[48:63], v[124:127], v[124:127], 0
	v_mfma_f32_32x32x16_bf16 v[64:79], v[124:127], v[124:127], 0
	v_mfma_f32_32x32x16_bf16 v[80:95], v[124:127], v[124:127], 0
	v_mfma_f32_32x32x16_bf16 v[96:111], v[124:127], v[124:127], 0
	v_mfma_f32_16x16x32_bf16 v[112:115], v[124:127], v[124:127], 0
	v_mfma_f32_16x16x32_bf16 v[116:119], v[124:127], v[124:127], 0
	v_mfma_f32_16x16x32_bf16 v[120:123], v[124:127], v[124:127], 0
	s_add_i32 s74, s74, 1
	s_mul_i32 s4, s74, s92
	s_mul_hi_u32 s5, s74, s34
	s_add_i32 s5, s5, s4
	s_mul_i32 s4, s74, s34
	s_add_u32 s58, s4, s2
	s_addc_u32 s59, s5, s36
	v_cmp_gt_i64_e32 vcc, s[58:59], v[130:131]
	v_cmp_lt_i64_e64 s[4:5], s[58:59], v[128:129]
	s_cbranch_vccnz .LBB0_723
	s_ashr_i32 s54, s58, 31
	s_lshr_b32 s54, s54, 29
	s_add_i32 s56, s58, s54
	s_and_b32 s54, s56, -8
	s_sub_i32 s57, s58, s54
	s_cmp_gt_i32 s57, -1
	s_mov_b64 s[54:55], -1
	s_cbranch_scc0 .LBB0_720
	s_lshl_b32 s58, s57, 5
	s_mov_b64 s[54:55], 0

; #define PG8_BAR __builtin_amdgcn_s_barrier()
;     DI int nt(const Unit& u) const { return (u.aux & 8) ? PLED / 64 : ((u.aux & 4) ? (D_ / 2) / 64 : D_ / 64); }
; template <class Epi, class Sched, bool ALIGN_EPI, bool FP8 = false>
; DI void gemm_phase(LAS unsigned char* lds, const Gemm g, const Sched& S, const Epi& E) {
;     ...
; #pragma unroll
;         for (int a = 0; a < 2; ++a)
; #pragma unroll
;             for (int b = 0; b < 2; ++b)
; #pragma unroll
;                 for (int m = 0; m < 4; ++m)
; #pragma unroll
;                     for (int n = 0; n < 2; ++n) acc[a][b][m][n] = (f32x4){0.f, 0.f, 0.f, 0.f};
;         cur = nxt; cA = nA; cB = nB; ++ui;
;         if constexpr (sched_vark<Sched>::value) nt = S.nt(cur);
;         if constexpr (ALIGN_EPI) { if (wr == 1) PG8_BAR; }
.LBB0_723:
	s_ashr_i32 s57, s56, 31
	s_lshl_b64 s[58:59], s[56:57], 20
	s_add_u32 s58, s3, s58
	s_addc_u32 s59, s35, s59
	s_and_b64 s[60:61], s[4:5], exec
	s_cselect_b32 s57, s59, s65
	s_cselect_b32 s94, s58, s64
	s_ashr_i32 s55, s54, 31
	s_lshl_b64 s[60:61], s[54:55], 20
	s_add_u32 s60, s37, s60
	s_addc_u32 s61, s39, s61
	s_and_b64 s[68:69], s[4:5], exec
	s_cselect_b32 s55, s61, s67
	s_cselect_b32 s95, s60, s66
	s_add_u32 s96, s66, 0x100
	s_addc_u32 s97, s67, 0
	s_mov_b32 vcc_lo, -2
	s_waitcnt vmcnt(15)
	s_waitcnt vmcnt(14)
	s_waitcnt vmcnt(13)
	s_waitcnt vmcnt(12)
	s_waitcnt vmcnt(11)
	s_waitcnt vmcnt(9)
	s_waitcnt vmcnt(8)
	.p2alignl 6, 3212836864

; #define PG8_BAR __builtin_amdgcn_s_barrier()
;     DI bool next(int i, Unit& u) const { u.aux = 0; return tile_map(i, nM, nN, G, c, u.pm, u.pn); }
;     DI size_t a_off(const Unit& u) const { return (size_t)u.pm * astep; }
;     DI size_t b_off(const Unit& u) const { return (size_t)u.pn * bstep; }
;     DI bool next(int i, Unit& u) const { int pn; u.aux = 0; if (!tile_map(i, NTOK / 256, 16, G, c, u.pm, pn)) return false; u.pn = pn < 8 ? pn : pn + 8; return true; }
;     DI size_t a_off(const Unit& u) const { return (size_t)u.pm * (256 * D_ * 2); }
;     DI size_t b_off(const Unit& u) const { return (size_t)u.pn * (256 * D_ * 2); }
;     DI bool next(int i, Unit& u) const { int pn2; if (!tile_map(i, NTOK / 256, 8, G, c, u.pm, pn2)) return false; u.pn = pn2 >> 1; u.aux = pn2 & 1; return true; }
; DI bool tile_map(int i, int nM, int nN, int G, int c, int& pm, int& pn) {
;     const int nwg = nM * nN; const long L = (long)i * G + c; if (L >= nwg) return false;
;     int wgid = (int)L; { const int q = nwg / NXCD, r = nwg % NXCD, xcd = wgid % NXCD, off = wgid / NXCD; wgid = (xcd < r ? xcd * (q + 1) : r * (q + 1) + (xcd - r) * q) + off; }
;     const int nig = WGM * nN, gid = wgid / nig, fm = gid * WGM, gsz = (nM - fm) < WGM ? (nM - fm) : WGM;
;     pm = fm + ((wgid % nig) % gsz); pn = (wgid % nig) / gsz; return true;
; template <class Epi, class Sched, bool ALIGN_EPI, bool FP8 = false>
; DI void gemm_phase(LAS unsigned char* lds, const Gemm g, const Sched& S, const Epi& E) {
;     ...
;     for (;;) {
;         const bool has_next = S.next(ui + 1, nxt);
;         const char* nA = has_next ? (const char*)g.A + S.a_off(nxt) : cA; const char* nB = has_next ? (const char*)g.Bt + S.b_off(nxt) : cB;
;     ...
; #pragma unroll
;         for (int a = 0; a < 2; ++a)
; #pragma unroll
;             for (int b = 0; b < 2; ++b)
; #pragma unroll
;                 for (int m = 0; m < 4; ++m)
; #pragma unroll
;                     for (int n = 0; n < 2; ++n) acc[a][b][m][n] = (f32x4){0.f, 0.f, 0.f, 0.f};
;         cur = nxt; cA = nA; cB = nB; ++ui;
;         if constexpr (sched_vark<Sched>::value) nt = S.nt(cur);
;         if constexpr (ALIGN_EPI) { if (wr == 1) PG8_BAR; }
;     DI bool next(int i, Unit& u) const { if (!tile_map(i, nM, nN, G, c, u.pm, u.pn)) return false; u.aux = __builtin_amdgcn_readfirstlane(blk_e[u.pm]); return true; }
.LBB0_1603:
	v_mov_b32_e32 v124, 0
	v_mov_b32_e32 v125, 0
	v_mov_b32_e32 v126, 0
	v_mov_b32_e32 v127, 0
	s_nop 1
	v_mfma_f32_32x32x16_bf16 v[0:15], v[124:127], v[124:127], 0
	v_mfma_f32_32x32x16_bf16 v[16:31], v[124:127], v[124:127], 0
	v_mfma_f32_32x32x16_bf16 v[32:47], v[124:127], v[124:127], 0
	v_mfma_f32_32x32x16_bf16 v[48:63], v[124:127], v[124:127], 0
	v_mfma_f32_32x32x16_bf16 v[64:79], v[124:127], v[124:127], 0
	v_mfma_f32_32x32x16_bf16 v[80:95], v[124:127], v[124:127], 0
	v_mfma_f32_32x32x16_bf16 v[96:111], v[124:127], v[124:127], 0
	v_mfma_f32_16x16x32_bf16 v[112:115], v[124:127], v[124:127], 0
	v_mfma_f32_16x16x32_bf16 v[116:119], v[124:127], v[124:127], 0
	v_mfma_f32_16x16x32_bf16 v[120:123], v[124:127], v[124:127], 0
	s_add_i32 s55, s55, 1
	s_mul_i32 s4, s55, s64
	s_mul_hi_u32 s5, s55, s34
	s_add_i32 s5, s5, s4
	s_mul_i32 s4, s55, s34
	s_add_u32 s4, s4, s2
	s_addc_u32 s5, s5, s46
	v_cmp_ge_i64_e32 vcc, s[4:5], v[252:253]
	v_cmp_lt_i64_e64 s[6:7], s[4:5], v[252:253]
	s_cbranch_vccnz .LBB0_1605
	s_ashr_i32 s5, s4, 31
	s_lshr_b32 s5, s5, 29
	s_add_i32 s5, s4, s5
	s_ashr_i32 s14, s5, 3
	s_and_b32 s5, s5, -8
	s_sub_i32 s4, s4, s5
	s_cmp_lt_i32 s4, 0
	s_cselect_b32 s5, s47, s45
	s_mul_i32 s4, s5, s4
	s_add_i32 s4, s4, s14
	s_mul_hi_i32 s5, s4, 0x92492493
	s_add_i32 s5, s5, s4
	s_lshr_b32 s14, s5, 31
	s_ashr_i32 s5, s5, 8
	s_add_i32 s5, s5, s14
	s_lshl_b32 s15, s5, 3
	s_sub_i32 s14, s3, s15
	s_min_i32 s16, s14, 8
	s_abs_i32 s14, s16
	v_cvt_f32_u32_e32 v255, s14
	s_sub_i32 s18, 0, s14
	s_mulk_i32 s5, 0x1c0
	s_sub_i32 s4, s4, s5
	v_rcp_iflag_f32_e32 v255, v255
	s_abs_i32 s5, s4
	s_xor_b32 s17, s4, s16
	s_ashr_i32 s17, s17, 31
	v_mul_f32_e32 v255, 0x4f7ffffe, v255
	v_cvt_u32_f32_e32 v255, v255
	s_nop 0
	v_readfirstlane_b32 s19, v255
	s_mul_i32 s18, s18, s19
	s_mul_hi_u32 s18, s19, s18
	s_add_i32 s19, s19, s18
	s_mul_hi_u32 s18, s5, s19
	s_mul_i32 s19, s18, s14
	s_sub_i32 s5, s5, s19
	s_add_i32 s20, s18, 1
	s_sub_i32 s19, s5, s14
	s_cmp_ge_u32 s5, s14
	s_cselect_b32 s18, s20, s18
	s_cselect_b32 s5, s19, s5
	s_add_i32 s19, s18, 1
	s_cmp_ge_u32 s5, s14
	s_cselect_b32 s5, s19, s18
	s_xor_b32 s5, s5, s17
	s_sub_i32 s14, s5, s17
	s_mul_i32 s5, s14, s16
	s_sub_i32 s4, s4, s5
	s_add_i32 s16, s4, s15
	s_lshl_b32 s4, s16, 2
	s_add_i32 s4, s4, 0
	s_add_i32 s4, s4, 0x20400
	v_mov_b32_e32 v255, s4
	ds_read_b32 v255, v255
	s_waitcnt lgkmcnt(0)
	v_readfirstlane_b32 s67, v255
.LBB0_1605:
	s_nop 0
	v_cndmask_b32_e64 v255, 0, 1, s[6:7]
	v_cmp_ne_u32_e64 s[4:5], 1, v255
	s_andn2_b64 vcc, exec, s[6:7]
	s_mov_b64 s[18:19], s[28:29]
	s_cbranch_vccnz .LBB0_1607
	s_ashr_i32 s15, s14, 31
	s_mul_i32 s20, s67, 0x1c00000
	s_lshl_b64 s[18:19], s[14:15], 19
	s_mul_hi_i32 s17, s67, 0x1c00000
	s_add_u32 s15, s37, s20
	s_addc_u32 s17, s39, s17
	s_add_u32 s18, s15, s18
	s_addc_u32 s19, s17, s19
.LBB0_1607:
	s_ashr_i32 s17, s16, 31
	s_lshl_b64 s[20:21], s[16:17], 19
	s_add_u32 s20, s35, s20
	s_addc_u32 s21, s36, s21
	s_and_b64 s[6:7], s[6:7], exec
	s_cselect_b32 s15, s21, s27
	s_cselect_b32 s17, s20, s26
	s_add_u32 s68, s28, 0x100
	s_addc_u32 s69, s29, 0
	s_mov_b32 s70, -2
	.p2alignl 6, 3212836864

;     DI bool next(int i, Unit& u) const { u.aux = 0; return tile_map(i, nM, nN, G, c, u.pm, u.pn); }
;     DI size_t a_off(const Unit& u) const { return (size_t)u.pm * astep; }
;     DI size_t b_off(const Unit& u) const { return (size_t)u.pn * bstep; }
;     DI bool next(int i, Unit& u) const { int pn; u.aux = 0; if (!tile_map(i, NTOK / 256, 16, G, c, u.pm, pn)) return false; u.pn = pn < 8 ? pn : pn + 8; return true; }
;     DI size_t a_off(const Unit& u) const { return (size_t)u.pm * (256 * D_ * 2); }
;     DI size_t b_off(const Unit& u) const { return (size_t)u.pn * (256 * D_ * 2); }
;     DI bool next(int i, Unit& u) const { int pn2; if (!tile_map(i, NTOK / 256, 8, G, c, u.pm, pn2)) return false; u.pn = pn2 >> 1; u.aux = pn2 & 1; return true; }
;     DI size_t a_off(const Unit& u) const { return (size_t)u.pm * (256 * D_ * 2) + (size_t)u.aux * (D_ / 2 * 2); }
;     DI size_t b_off(const Unit& u) const { return (size_t)(12 + u.pn) * (256 * D_ * 2) + (size_t)u.aux * (D_ / 2 * 2); }
;     DI bool next(int i, Unit& u) const { u.aux = 0; return tile_map(i, 8, NTOK / 256, G, c, u.pm, u.pn); }
;     DI size_t a_off(const Unit& u) const { const int phys = u.pm < 4 ? 8 + u.pm : 20 + u.pm; return (size_t)phys * (256 * D_ * 2); }
;     DI size_t b_off(const Unit& u) const { return (size_t)u.pn * (256 * D_ * 2); }
; DI bool tile_map(int i, int nM, int nN, int G, int c, int& pm, int& pn) {
;     const int nwg = nM * nN; const long L = (long)i * G + c; if (L >= nwg) return false;
;     int wgid = (int)L; { const int q = nwg / NXCD, r = nwg % NXCD, xcd = wgid % NXCD, off = wgid / NXCD; wgid = (xcd < r ? xcd * (q + 1) : r * (q + 1) + (xcd - r) * q) + off; }
;     const int nig = WGM * nN, gid = wgid / nig, fm = gid * WGM, gsz = (nM - fm) < WGM ? (nM - fm) : WGM;
;     pm = fm + ((wgid % nig) % gsz); pn = (wgid % nig) / gsz; return true;
; template <class Epi, class Sched, bool ALIGN_EPI, bool FP8 = false>
; DI void gemm_phase(LAS unsigned char* lds, const Gemm g, const Sched& S, const Epi& E) {
;     ...
;     for (;;) {
;         const bool has_next = S.next(ui + 1, nxt);
;         const char* nA = has_next ? (const char*)g.A + S.a_off(nxt) : cA; const char* nB = has_next ? (const char*)g.Bt + S.b_off(nxt) : cB;
;     DI bool next(int i, Unit& u) const { if (!tile_map(i, nM, nN, G, c, u.pm, u.pn)) return false; u.aux = __builtin_amdgcn_readfirstlane(blk_e[u.pm]); return true; }
.LBB0_1678:
	v_mov_b32_e32 v124, 0
	v_mov_b32_e32 v125, 0
	v_mov_b32_e32 v126, 0
	v_mov_b32_e32 v127, 0
	s_nop 1
	v_mfma_f32_32x32x16_bf16 v[0:15], v[124:127], v[124:127], 0
	v_mfma_f32_32x32x16_bf16 v[16:31], v[124:127], v[124:127], 0
	v_mfma_f32_32x32x16_bf16 v[32:47], v[124:127], v[124:127], 0
	v_mfma_f32_32x32x16_bf16 v[48:63], v[124:127], v[124:127], 0
	v_mfma_f32_32x32x16_bf16 v[64:79], v[124:127], v[124:127], 0
	v_mfma_f32_32x32x16_bf16 v[80:95], v[124:127], v[124:127], 0
	v_mfma_f32_32x32x16_bf16 v[96:111], v[124:127], v[124:127], 0
	v_mfma_f32_16x16x32_bf16 v[112:115], v[124:127], v[124:127], 0
	v_mfma_f32_16x16x32_bf16 v[116:119], v[124:127], v[124:127], 0
	v_mfma_f32_16x16x32_bf16 v[120:123], v[124:127], v[124:127], 0
	s_add_i32 s66, s66, 1
	s_mul_i32 s4, s66, s75
	s_mul_hi_u32 s5, s66, s34
	s_add_i32 s5, s5, s4
	s_mul_i32 s4, s66, s34
	s_add_u32 s4, s4, s2
	s_addc_u32 s5, s5, s55
	v_cmp_ge_i64_e32 vcc, s[4:5], v[128:129]
	v_cmp_lt_i64_e64 s[6:7], s[4:5], v[128:129]
	s_cbranch_vccnz .LBB0_1680
	s_ashr_i32 s5, s4, 31
	s_lshr_b32 s5, s5, 29
	s_add_i32 s5, s4, s5
	s_ashr_i32 s42, s5, 3
	s_and_b32 s5, s5, -8
	s_sub_i32 s4, s4, s5
	s_cmp_lt_i32 s4, 0
	s_cselect_b32 s5, s56, s3
	s_mul_i32 s4, s5, s4
	s_add_i32 s4, s4, s42
	s_ashr_i32 s5, s4, 31
	s_lshr_b32 s5, s5, 26
	s_add_i32 s5, s4, s5
	s_ashr_i32 s42, s5, 6
	s_lshl_b32 s42, s42, 3
	s_sub_i32 s43, s3, s42
	s_min_i32 s43, s43, 8
	s_abs_i32 s48, s43
	v_cvt_f32_u32_e32 v255, s48
	s_sub_i32 s50, 0, s48
	s_andn2_b32 s5, s5, 63
	s_sub_i32 s4, s4, s5
	v_rcp_iflag_f32_e32 v255, v255
	s_abs_i32 s5, s4
	s_xor_b32 s49, s4, s43
	s_ashr_i32 s49, s49, 31
	v_mul_f32_e32 v255, 0x4f7ffffe, v255
	v_cvt_u32_f32_e32 v255, v255
	s_nop 0
	v_readfirstlane_b32 s51, v255
	s_mul_i32 s50, s50, s51
	s_mul_hi_u32 s50, s51, s50
	s_add_i32 s51, s51, s50
	s_mul_hi_u32 s50, s5, s51
	s_mul_i32 s51, s50, s48
	s_sub_i32 s5, s5, s51
	s_add_i32 s52, s50, 1
	s_sub_i32 s51, s5, s48
	s_cmp_ge_u32 s5, s48
	s_cselect_b32 s50, s52, s50
	s_cselect_b32 s5, s51, s5
	s_add_i32 s51, s50, 1
	s_cmp_ge_u32 s5, s48
	s_cselect_b32 s5, s51, s50
	s_xor_b32 s5, s5, s49
	s_sub_i32 s84, s5, s49
	s_mul_i32 s5, s84, s43
	s_sub_i32 s4, s4, s5
	s_add_i32 s85, s4, s42
	s_lshl_b32 s4, s85, 2
	s_add_i32 s4, s4, 0
	s_add_i32 s4, s4, 0x20400
	v_mov_b32_e32 v255, s4
	ds_read_b32 v255, v255
	s_waitcnt lgkmcnt(0)
	v_readfirstlane_b32 s86, v255
.LBB0_1680:
	s_nop 0
	v_cndmask_b32_e64 v255, 0, 1, s[6:7]
	v_cmp_ne_u32_e64 s[4:5], 1, v255
	s_andn2_b64 vcc, exec, s[6:7]
	s_mov_b64 s[6:7], s[44:45]
	s_cbranch_vccnz .LBB0_1682
	s_mul_i32 s6, s85, 0x1c0000
	s_mul_hi_i32 s7, s85, 0x1c0000
	s_add_u32 s6, s35, s6
	s_addc_u32 s7, s36, s7

; #define PG8_BAR __builtin_amdgcn_s_barrier()
;     DI int nt(const Unit& u) const { return (u.aux & 8) ? PLED / 64 : ((u.aux & 4) ? (D_ / 2) / 64 : D_ / 64); }
; template <class Epi, class Sched, bool ALIGN_EPI, bool FP8 = false>
; DI void gemm_phase(LAS unsigned char* lds, const Gemm g, const Sched& S, const Epi& E) {
;     ...
; #pragma unroll
;         for (int a = 0; a < 2; ++a)
; #pragma unroll
;             for (int b = 0; b < 2; ++b)
; #pragma unroll
;                 for (int m = 0; m < 4; ++m)
; #pragma unroll
;                     for (int n = 0; n < 2; ++n) acc[a][b][m][n] = (f32x4){0.f, 0.f, 0.f, 0.f};
;         cur = nxt; cA = nA; cB = nB; ++ui;
;         if constexpr (sched_vark<Sched>::value) nt = S.nt(cur);
;         if constexpr (ALIGN_EPI) { if (wr == 1) PG8_BAR; }
.LBB0_1684:
	s_add_u32 s90, s46, 0x100
	s_addc_u32 s91, s47, 0
	s_mov_b32 s92, -2
	.p2alignl 6, 3212836864

;     DI bool next(int i, Unit& u) const { u.aux = 0; return tile_map(i, nM, nN, G, c, u.pm, u.pn); }
;     DI size_t a_off(const Unit& u) const { return (size_t)u.pm * astep; }
;     DI size_t b_off(const Unit& u) const { return (size_t)u.pn * bstep; }
;     DI bool next(int i, Unit& u) const { int pn; u.aux = 0; if (!tile_map(i, NTOK / 256, 16, G, c, u.pm, pn)) return false; u.pn = pn < 8 ? pn : pn + 8; return true; }
;     DI size_t a_off(const Unit& u) const { return (size_t)u.pm * (256 * D_ * 2); }
;     DI size_t b_off(const Unit& u) const { return (size_t)u.pn * (256 * D_ * 2); }
;     DI bool next(int i, Unit& u) const { int pn2; if (!tile_map(i, NTOK / 256, 8, G, c, u.pm, pn2)) return false; u.pn = pn2 >> 1; u.aux = pn2 & 1; return true; }
;     DI size_t a_off(const Unit& u) const { return (size_t)u.pm * (256 * D_ * 2) + (size_t)u.aux * (D_ / 2 * 2); }
;     DI size_t b_off(const Unit& u) const { return (size_t)(12 + u.pn) * (256 * D_ * 2) + (size_t)u.aux * (D_ / 2 * 2); }
;     DI bool next(int i, Unit& u) const { u.aux = 0; return tile_map(i, 8, NTOK / 256, G, c, u.pm, u.pn); }
;     DI size_t a_off(const Unit& u) const { const int phys = u.pm < 4 ? 8 + u.pm : 20 + u.pm; return (size_t)phys * (256 * D_ * 2); }
;     DI size_t b_off(const Unit& u) const { return (size_t)u.pn * (256 * D_ * 2); }
;     DI bool next(int i, Unit& u) const { u.aux = i & 1; return tile_map(i >> 1, NTOK / 256, D_ / 256, G, c, u.pm, u.pn); }
; DI bool tile_map(int i, int nM, int nN, int G, int c, int& pm, int& pn) {
;     const int nwg = nM * nN; const long L = (long)i * G + c; if (L >= nwg) return false;
;     int wgid = (int)L; { const int q = nwg / NXCD, r = nwg % NXCD, xcd = wgid % NXCD, off = wgid / NXCD; wgid = (xcd < r ? xcd * (q + 1) : r * (q + 1) + (xcd - r) * q) + off; }
;     const int nig = WGM * nN, gid = wgid / nig, fm = gid * WGM, gsz = (nM - fm) < WGM ? (nM - fm) : WGM;
;     pm = fm + ((wgid % nig) % gsz); pn = (wgid % nig) / gsz; return true;
; template <class Epi, class Sched, bool ALIGN_EPI, bool FP8 = false>
; DI void gemm_phase(LAS unsigned char* lds, const Gemm g, const Sched& S, const Epi& E) {
;     ...
;     for (;;) {
;         const bool has_next = S.next(ui + 1, nxt);
;         const char* nA = has_next ? (const char*)g.A + S.a_off(nxt) : cA; const char* nB = has_next ? (const char*)g.Bt + S.b_off(nxt) : cB;
.LBB0_1703:
	v_mov_b32_e32 v124, 0
	v_mov_b32_e32 v125, 0
	v_mov_b32_e32 v126, 0
	v_mov_b32_e32 v127, 0
	s_nop 1
	v_mfma_f32_32x32x16_bf16 v[0:15], v[124:127], v[124:127], 0
	v_mfma_f32_32x32x16_bf16 v[16:31], v[124:127], v[124:127], 0
	v_mfma_f32_32x32x16_bf16 v[32:47], v[124:127], v[124:127], 0
	v_mfma_f32_32x32x16_bf16 v[48:63], v[124:127], v[124:127], 0
	v_mfma_f32_32x32x16_bf16 v[64:79], v[124:127], v[124:127], 0
	v_mfma_f32_32x32x16_bf16 v[80:95], v[124:127], v[124:127], 0
	v_mfma_f32_32x32x16_bf16 v[96:111], v[124:127], v[124:127], 0
	v_mfma_f32_16x16x32_bf16 v[112:115], v[124:127], v[124:127], 0
	v_mfma_f32_16x16x32_bf16 v[116:119], v[124:127], v[124:127], 0
	v_mfma_f32_16x16x32_bf16 v[120:123], v[124:127], v[124:127], 0
	s_add_i32 s73, s73, 1
	s_mul_i32 s2, s73, s92
	s_mul_hi_u32 s3, s73, s91
	s_add_i32 s3, s3, s2
	s_mul_i32 s2, s73, s91
	s_add_u32 s56, s2, s35
	s_addc_u32 s57, s3, 0
	v_cmp_gt_i64_e32 vcc, s[56:57], v[130:131]
	v_cmp_lt_i64_e64 s[2:3], s[56:57], v[128:129]
	s_cbranch_vccnz .LBB0_1709
	s_ashr_i32 s52, s56, 31
	s_lshr_b32 s52, s52, 29
	s_add_i32 s54, s56, s52
	s_and_b32 s52, s54, -8
	s_sub_i32 s55, s56, s52
	s_cmp_gt_i32 s55, -1
	s_mov_b64 s[52:53], -1
	s_cbranch_scc0 .LBB0_1706
	s_lshl_b32 s56, s55, 5
	s_mov_b64 s[52:53], 0

; #define PG8_BAR __builtin_amdgcn_s_barrier()
;     DI int nt(const Unit& u) const { return (u.aux & 8) ? PLED / 64 : ((u.aux & 4) ? (D_ / 2) / 64 : D_ / 64); }
; DI bool tile_map(int i, int nM, int nN, int G, int c, int& pm, int& pn) {
;     const int nwg = nM * nN; const long L = (long)i * G + c; if (L >= nwg) return false;
;     int wgid = (int)L; { const int q = nwg / NXCD, r = nwg % NXCD, xcd = wgid % NXCD, off = wgid / NXCD; wgid = (xcd < r ? xcd * (q + 1) : r * (q + 1) + (xcd - r) * q) + off; }
;     const int nig = WGM * nN, gid = wgid / nig, fm = gid * WGM, gsz = (nM - fm) < WGM ? (nM - fm) : WGM;
;     pm = fm + ((wgid % nig) % gsz); pn = (wgid % nig) / gsz; return true;
; template <class Epi, class Sched, bool ALIGN_EPI, bool FP8 = false>
; DI void gemm_phase(LAS unsigned char* lds, const Gemm g, const Sched& S, const Epi& E) {
;     ...
; #pragma unroll
;         for (int a = 0; a < 2; ++a)
; #pragma unroll
;             for (int b = 0; b < 2; ++b)
; #pragma unroll
;                 for (int m = 0; m < 4; ++m)
; #pragma unroll
;                     for (int n = 0; n < 2; ++n) acc[a][b][m][n] = (f32x4){0.f, 0.f, 0.f, 0.f};
;         cur = nxt; cA = nA; cB = nB; ++ui;
;         if constexpr (sched_vark<Sched>::value) nt = S.nt(cur);
;         if constexpr (ALIGN_EPI) { if (wr == 1) PG8_BAR; }
.LBB0_1708:
	s_ashr_i32 s52, s54, 3
	s_add_i32 s52, s56, s52
	s_ashr_i32 s53, s52, 31
	s_lshr_b32 s53, s53, 26
	s_add_i32 s53, s52, s53
	s_ashr_i32 s54, s53, 6
	s_lshl_b32 s54, s54, 3
	s_sub_i32 s55, 32, s54
	s_min_i32 s55, s55, 8
	s_abs_i32 s56, s55
	v_cvt_f32_u32_e32 v255, s56
	s_sub_i32 s58, 0, s56
	s_andn2_b32 s53, s53, 63
	s_sub_i32 s53, s52, s53
	v_rcp_iflag_f32_e32 v255, v255
	s_abs_i32 s52, s53
	s_xor_b32 s57, s53, s55
	s_ashr_i32 s57, s57, 31
	v_mul_f32_e32 v255, 0x4f7ffffe, v255
	v_cvt_u32_f32_e32 v255, v255
	s_nop 0
	v_readfirstlane_b32 s59, v255
	s_mul_i32 s58, s58, s59
	s_mul_hi_u32 s58, s59, s58
	s_add_i32 s59, s59, s58
	s_mul_hi_u32 s58, s52, s59
	s_mul_i32 s59, s58, s56
	s_sub_i32 s52, s52, s59
	s_add_i32 s66, s58, 1
	s_sub_i32 s59, s52, s56
	s_cmp_ge_u32 s52, s56
	s_cselect_b32 s58, s66, s58
	s_cselect_b32 s52, s59, s52
	s_add_i32 s59, s58, 1
	s_cmp_ge_u32 s52, s56
	s_cselect_b32 s52, s59, s58
	s_xor_b32 s52, s52, s57
	s_sub_i32 s52, s52, s57
	s_mul_i32 s55, s52, s55
	s_sub_i32 s53, s53, s55
	s_add_i32 s54, s54, s53
.LBB0_1709:
	s_ashr_i32 s55, s54, 31
	s_lshl_b64 s[56:57], s[54:55], 20
	s_add_u32 s56, s36, s56
	s_addc_u32 s57, s37, s57
	s_and_b64 s[58:59], s[2:3], exec
	s_cselect_b32 s55, s57, s63
	s_cselect_b32 s94, s56, s62
	s_ashr_i32 s53, s52, 31
	s_lshl_b64 s[58:59], s[52:53], 20
	s_add_u32 s58, s39, s58
	s_addc_u32 s59, s72, s59
	s_and_b64 s[66:67], s[2:3], exec
	s_cselect_b32 s53, s59, s65
	s_cselect_b32 s95, s58, s64
	s_add_u32 s96, s64, 0x100
	s_addc_u32 s97, s65, 0
	s_mov_b32 vcc_lo, -2
	.p2alignl 6, 3212836864
